# indexer: one static priority raise (s_setprio 1) for waves 4-7 for the whole phase, reset at phase exit
# baseline (speedup 1.0000x reference)
.LBB0_1149:
	v_mov_b32_e32 v1, 0x27ff0
	v_mov_b32_e32 v8, v0
	v_add_u32_e32 v1, 0, v1
	ds_read2_b32 v[2:3], v1 offset1:1
	ds_read2_b32 v[4:5], v1 offset0:2 offset1:3
	s_waitcnt lgkmcnt(0)
	s_barrier
	s_load_dword s61, s[16:17], 0x0
	s_cmp_eq_u32 s53, 0
	v_readfirstlane_b32 s4, v8
	s_cselect_b64 s[2:3], -1, 0
	s_ashr_i32 s54, s4, 6
	s_ashr_i32 s4, s4, 8
	s_cmp_lt_u32 s54, 4
	s_cbranch_scc1 .Lprio_lo
	s_setprio 1
.Lprio_lo:
	s_nop 0
	s_nop 0
	s_nop 0
	s_nop 0
	s_nop 0
	s_nop 0
	s_nop 0
	s_nop 0
	s_nop 0
	s_nop 0
	s_nop 0
	s_nop 0
	s_nop 0
	v_and_b32_e32 v9, 31, v8
	v_bfe_u32 v1, v8, 3, 3
	v_bfe_u32 v10, v8, 5, 1
	v_lshl_or_b32 v6, s54, 3, v1
	v_lshlrev_b32_e32 v1, 7, v9
	v_lshrrev_b32_e32 v7, 1, v8
	s_waitcnt lgkmcnt(0)
	s_cmpk_lg_i32 s61, 0x100
	v_lshl_or_b32 v1, s4, 12, v1
	v_bfe_u32 v12, v8, 1, 3
	v_bitop3_b32 v7, v10, v7, 7 bitop3:0x78
	s_cselect_b64 s[22:23], -1, 0
	s_lshl_b32 s6, s54, 1
	v_lshl_or_b32 v111, v7, 4, v1
	v_bitop3_b32 v7, v10, v12, 2 bitop3:0x36
	v_readfirstlane_b32 s55, v2
	s_and_b32 s62, s6, 6
	v_bfe_u32 v2, v8, 4, 1
	v_lshl_or_b32 v112, v7, 4, v1
	v_bitop3_b32 v7, v10, v12, 4 bitop3:0x36
	v_or_b32_e32 v115, s62, v2
	v_lshlrev_b32_e32 v2, 7, v8
	v_lshrrev_b32_e32 v11, 1, v6
	v_lshl_or_b32 v113, v7, 4, v1
	v_bitop3_b32 v7, v10, v12, 6 bitop3:0x36
	v_and_b32_e32 v94, 0x780, v2
	v_lshl_or_b32 v114, v7, 4, v1
	v_readfirstlane_b32 s56, v3
	v_xor_b32_e32 v1, v11, v8
	v_lshl_add_u64 v[2:3], s[72:73], 0, v[94:95]
	v_lshlrev_b32_e32 v94, 4, v10
	v_ashrrev_i32_e32 v7, 31, v6
	s_lshl_b32 s7, s54, 12
	v_lshl_add_u64 v[96:97], v[2:3], 0, v[94:95]
	v_lshlrev_b64 v[2:3], 7, v[6:7]
	v_lshlrev_b32_e32 v1, 4, v1
	s_add_i32 s63, s7, 0
	s_mul_i32 s8, s54, 0xfffff400
	v_readfirstlane_b32 s57, v4
	v_readfirstlane_b32 s60, v5
	v_lshl_add_u64 v[4:5], s[78:79], 0, v[2:3]
	v_and_b32_e32 v6, 0x70, v1
	v_mov_b32_e32 v7, v95
	s_lshl_b32 s6, s4, 6
	s_add_i32 s10, s63, s8
	s_lshl_b32 s4, s4, 5
	s_or_b64 s[24:25], s[2:3], s[82:83]
	s_lshl_b32 s2, s54, 9
	v_and_b32_e32 v110, 63, v8
	v_lshl_add_u64 v[98:99], v[4:5], 0, v[6:7]
	s_sub_i32 s52, s10, s2
	v_lshlrev_b64 v[4:5], v8, -1
	s_add_i32 s2, s4, 0xc0
	v_not_b32_e32 v1, v5
	v_not_b32_e32 v100, v4
	v_lshlrev_b32_e32 v4, 3, v110
	v_mov_b32_e32 v5, v95
	v_lshl_add_u64 v[104:105], s[76:77], 0, v[94:95]
	v_or_b32_e32 v94, s2, v9
	s_lshl_b32 s2, s54, 13
	v_lshl_add_u64 v[102:103], s[80:81], 0, v[4:5]
	v_bitop3_b32 v5, v11, 7, v8 bitop3:0x48
	s_and_b32 s2, s2, 0x6000
	v_lshl_or_b32 v2, v5, 4, v2
	s_add_i32 s6, s6, s2
	v_lshl_add_u64 v[106:107], s[46:47], 0, v[2:3]
	v_lshl_add_u32 v2, v10, 12, s6
	s_add_i32 s2, s4, 0x8c0
	s_lshl_b32 s7, s54, 10
	v_add_u32_e32 v118, s52, v4
	v_lshlrev_b16_e32 v119, 3, v110
	v_mul_i32_i24_e32 v4, -6, v110
	v_lshl_or_b32 v2, v9, 1, v2
	v_or_b32_e32 v251, s2, v9
	s_add_i32 s2, s4, 0x10c0
	s_addk_i32 s4, 0x18c0
	v_or_b32_e32 v116, s62, v10
	v_lshlrev_b32_e32 v117, 4, v110
	v_or_b32_e32 v247, 64, v110
	v_or_b32_e32 v248, 0x80, v110
	v_or_b32_e32 v249, 0xc0, v110
	s_add_i32 s20, s7, 0
	v_add_u32_e32 v139, 0, v2
	v_or_b32_e32 v252, s2, v9
	v_or_b32_e32 v138, s4, v9
	s_add_i32 s21, s10, 0x8000
	s_add_i32 s6, s10, 0xa000
	s_add_i32 s7, s10, 0xc000
	s_add_i32 s10, s10, 0xe000
	v_add_u32_e32 v128, v118, v4
	s_mov_b32 s11, s19
	s_branch .LBB0_1153

.LBB0_1856:
	s_setprio 0
	s_nop 0
	s_nop 0
	s_nop 0
	s_nop 0
	s_nop 0
	s_nop 0
	s_nop 0
	s_nop 0
	s_nop 0
	s_nop 0
	s_nop 0
	s_nop 0
	s_nop 0
	s_nop 0
	s_nop 0
	s_waitcnt vmcnt(0)
	s_barrier
	s_mov_b64 s[2:3], exec
	v_readlane_b32 s4, v253, 0
	v_readlane_b32 s5, v253, 1
	s_and_b64 s[4:5], s[2:3], s[4:5]
	s_mov_b64 exec, s[4:5]
	s_cbranch_execz .LBB0_1908
	s_add_i32 s4, 0, 0x27ff0
	v_mov_b32_e32 v1, s4
	s_waitcnt vmcnt(0) expcnt(0) lgkmcnt(0)
	ds_read_b32 v3, v1
	s_add_i32 s4, 0, 0x27ff4
	v_mov_b32_e32 v1, s4
	ds_read_b32 v1, v1
	s_waitcnt lgkmcnt(1)
	v_cmp_ne_u32_e32 vcc, 0, v3
	s_cbranch_vccnz .LBB0_1872
	s_load_dwordx2 s[4:5], s[0:1], 0x158
	s_load_dword s9, s[0:1], 0x160
	s_add_u32 s6, s46, 0x1000
	s_addc_u32 s7, s47, 0
	s_add_u32 s8, s46, 0x1100
	s_waitcnt lgkmcnt(0)
	s_mul_i32 s4, s5, s4
	s_mul_i32 s4, s4, s9
	s_addc_u32 s9, s47, 0
	s_add_u32 s10, s46, 0x1200
	s_addc_u32 s11, s47, 0
	s_add_u32 s12, s46, 0x1300
	s_addc_u32 s13, s47, 0
	s_mov_b32 s5, 1
	v_mov_b32_e32 v17, 0
	s_branch .LBB0_1860
